# w1v2
# baseline (speedup 1.0000x reference)
.Lw1f8:
	v_lshrrev_b32_e32 v1, 6, v7
	v_and_b32_e32 v2, 31, v0
	v_bfe_u32 v3, v0, 5, 1
	v_lshlrev_b32_e32 v5, 4, v7
	v_readfirstlane_b32 s10, v1
	v_cmp_ne_u32_e32 vcc, 0, v3
	s_and_b32 s11, s10, 1
	s_bfe_u32 s12, s10, 0x20001
	s_lshr_b32 s13, s10, 3
	s_lshl_b32 s13, s13, 2
	s_lshl1_add_u32 s16, s11, s13
	s_lshl_b32 s12, s12, 7
	v_lshl_add_u32 v4, v2, 2, s12
	v_mov_b32_e32 v8, 0x41800000
	v_mov_b32_e32 v9, 0x41000000
	v_mov_b32_e32 v10, 0
	v_cndmask_b32_e32 v9, v8, v9, vcc
	v_cndmask_b32_e32 v10, v8, v10, vcc
	s_waitcnt lgkmcnt(0)
	s_cmp_eq_u32 s16, 0
	s_cbranch_scc1 .Lw1_A
	s_cmp_eq_u32 s16, 20
	s_cbranch_scc1 .Lw1_B
	s_cmp_eq_u32 s16, 22
	s_cbranch_scc1 .Lw1_C
	s_mov_b32 s21, 0xa800
	v_mad_u32_u24 v11, v3, s21, v4
	s_lshl_b32 s20, s16, 11
	v_add_u32_e32 v11, s20, v11
	v_add_u32_e32 v6, 0x2c00, v11
	global_load_dword v16, v6, s[8:9]
	v_add_u32_e32 v6, 0x17000, v11
	global_load_dword v17, v6, s[8:9]
	v_add_u32_e32 v6, 0x2e00, v11
	global_load_dword v18, v6, s[8:9]
	v_add_u32_e32 v6, 0x17200, v11
	global_load_dword v19, v6, s[8:9]
	v_add_u32_e32 v6, 0x3000, v11
	global_load_dword v20, v6, s[8:9]
	v_add_u32_e32 v6, 0x17400, v11
	global_load_dword v21, v6, s[8:9]
	v_add_u32_e32 v6, 0x3200, v11
	global_load_dword v22, v6, s[8:9]
	v_add_u32_e32 v6, 0x17600, v11
	global_load_dword v23, v6, s[8:9]
	v_add_u32_e32 v6, 0x3400, v11
	global_load_dword v24, v6, s[8:9]
	v_add_u32_e32 v6, 0x17800, v11
	global_load_dword v25, v6, s[8:9]
	v_add_u32_e32 v6, 0x3600, v11
	global_load_dword v26, v6, s[8:9]
	v_add_u32_e32 v6, 0x17a00, v11
	global_load_dword v27, v6, s[8:9]
	v_add_u32_e32 v6, 0x3800, v11
	global_load_dword v28, v6, s[8:9]
	v_add_u32_e32 v6, 0x17c00, v11
	global_load_dword v29, v6, s[8:9]
	v_add_u32_e32 v6, 0x3a00, v11
	global_load_dword v30, v6, s[8:9]
	v_add_u32_e32 v6, 0x17e00, v11
	global_load_dword v31, v6, s[8:9]
	s_waitcnt vmcnt(15)
	v_mul_f32_e32 v16, 0x41800000, v16
	s_waitcnt vmcnt(14)
	v_mul_f32_e32 v17, 0x41000000, v17
	s_waitcnt vmcnt(13)
	v_mul_f32_e32 v18, 0x41800000, v18
	s_waitcnt vmcnt(12)
	v_mul_f32_e32 v19, 0x41000000, v19
	s_waitcnt vmcnt(11)
	v_mul_f32_e32 v20, 0x41800000, v20
	s_waitcnt vmcnt(10)
	v_mul_f32_e32 v21, 0x41000000, v21
	s_waitcnt vmcnt(9)
	v_mul_f32_e32 v22, 0x41800000, v22
	s_waitcnt vmcnt(8)
	v_mul_f32_e32 v23, 0x41000000, v23
	s_waitcnt vmcnt(7)
	v_mul_f32_e32 v24, 0x41800000, v24
	s_waitcnt vmcnt(6)
	v_mul_f32_e32 v25, 0x41000000, v25
	s_waitcnt vmcnt(5)
	v_mul_f32_e32 v26, 0x41800000, v26
	s_waitcnt vmcnt(4)
	v_mul_f32_e32 v27, 0x41000000, v27
	s_waitcnt vmcnt(3)
	v_mul_f32_e32 v28, 0x41800000, v28
	s_waitcnt vmcnt(2)
	v_mul_f32_e32 v29, 0x41000000, v29
	s_waitcnt vmcnt(1)
	v_mul_f32_e32 v30, 0x41800000, v30
	s_waitcnt vmcnt(0)
	v_mul_f32_e32 v31, 0x41000000, v31
	v_cvt_pk_fp8_f32 v0, v16, v17
	v_cvt_pk_fp8_f32 v1, v20, v21
	v_cvt_pk_fp8_f32 v2, v24, v25
	v_cvt_pk_fp8_f32 v3, v28, v29
	v_cvt_pk_fp8_f32 v0, v18, v19 op_sel:[0,0,1]
	v_cvt_pk_fp8_f32 v1, v22, v23 op_sel:[0,0,1]
	v_cvt_pk_fp8_f32 v2, v26, v27 op_sel:[0,0,1]
	v_cvt_pk_fp8_f32 v3, v30, v31 op_sel:[0,0,1]
	s_nop 1
	global_store_dwordx4 v5, v[0:3], s[6:7]
	s_endpgm
.Lw1_A:
	s_mov_b32 s21, 0x1c00
	v_mad_u32_u24 v11, v3, s21, v4
	s_mov_b32 s21, 0x14400
	v_mad_u32_u24 v12, v3, s21, v4
	v_mov_b32_e32 v6, v11
	global_load_dword v16, v6, s[8:9]
	v_add_u32_e32 v6, 0x200, v11
	global_load_dword v17, v6, s[8:9]
	v_add_u32_e32 v6, 0x400, v11
	global_load_dword v18, v6, s[8:9]
	v_add_u32_e32 v6, 0x600, v11
	global_load_dword v19, v6, s[8:9]
	v_add_u32_e32 v6, 0x800, v11
	global_load_dword v20, v6, s[8:9]
	v_add_u32_e32 v6, 0xa00, v11
	global_load_dword v21, v6, s[8:9]
	v_add_u32_e32 v6, 0xc00, v11
	global_load_dword v22, v6, s[8:9]
	v_add_u32_e32 v6, 0xe00, v11
	global_load_dword v23, v6, s[8:9]
	v_add_u32_e32 v6, 0x1000, v11
	global_load_dword v24, v6, s[8:9]
	v_add_u32_e32 v6, 0x1200, v11
	global_load_dword v25, v6, s[8:9]
	v_add_u32_e32 v6, 0x1400, v11
	global_load_dword v26, v6, s[8:9]
	v_add_u32_e32 v6, 0x1600, v11
	global_load_dword v27, v6, s[8:9]
	v_add_u32_e32 v6, 0x1800, v11
	global_load_dword v28, v6, s[8:9]
	v_add_u32_e32 v6, 0xd800, v12
	global_load_dword v29, v6, s[8:9]
	v_add_u32_e32 v6, 0xda00, v12
	global_load_dword v30, v6, s[8:9]
	v_add_u32_e32 v6, 0xdc00, v12
	global_load_dword v31, v6, s[8:9]
	s_waitcnt vmcnt(15)
	v_mul_f32_e32 v16, 0x41800000, v16
	s_waitcnt vmcnt(14)
	v_mul_f32_e32 v17, 0x41800000, v17
	s_waitcnt vmcnt(13)
	v_mul_f32_e32 v18, 0x41800000, v18
	s_waitcnt vmcnt(12)
	v_mul_f32_e32 v19, 0x41800000, v19
	s_waitcnt vmcnt(11)
	v_mul_f32_e32 v20, 0x41800000, v20
	s_waitcnt vmcnt(10)
	v_mul_f32_e32 v21, 0x41800000, v21
	s_waitcnt vmcnt(9)
	v_mul_f32_e32 v22, 0x41800000, v22
	s_waitcnt vmcnt(8)
	v_mul_f32_e32 v23, 0x41800000, v23
	s_waitcnt vmcnt(7)
	v_mul_f32_e32 v24, 0x41800000, v24
	s_waitcnt vmcnt(6)
	v_mul_f32_e32 v25, 0x41800000, v25
	s_waitcnt vmcnt(5)
	v_mul_f32_e32 v26, 0x41800000, v26
	s_waitcnt vmcnt(4)
	v_mul_f32_e32 v27, 0x41800000, v27
	s_waitcnt vmcnt(3)
	v_mul_f32_e32 v28, 0x41800000, v28
	s_waitcnt vmcnt(2)
	v_mul_f32_e32 v29, v9, v29
	s_waitcnt vmcnt(1)
	v_mul_f32_e32 v30, v9, v30
	s_waitcnt vmcnt(0)
	v_mul_f32_e32 v31, v9, v31
	v_cvt_pk_fp8_f32 v0, v16, v17
	v_cvt_pk_fp8_f32 v1, v20, v21
	v_cvt_pk_fp8_f32 v2, v24, v25
	v_cvt_pk_fp8_f32 v3, v28, v29
	v_cvt_pk_fp8_f32 v0, v18, v19 op_sel:[0,0,1]
	v_cvt_pk_fp8_f32 v1, v22, v23 op_sel:[0,0,1]
	v_cvt_pk_fp8_f32 v2, v26, v27 op_sel:[0,0,1]
	v_cvt_pk_fp8_f32 v3, v30, v31 op_sel:[0,0,1]
	s_nop 1
	global_store_dwordx4 v5, v[0:3], s[6:7]
	s_endpgm
.Lw1_B:
	s_mov_b32 s21, 0xa800
	v_mad_u32_u24 v11, v3, s21, v4
	s_mov_b32 s21, 0x14400
	v_mad_u32_u24 v12, v3, s21, v4
	v_add_u32_e32 v6, 0xcc00, v11
	global_load_dword v16, v6, s[8:9]
	v_add_u32_e32 v6, 0x21000, v11
	global_load_dword v17, v6, s[8:9]
	v_add_u32_e32 v6, 0xce00, v11
	global_load_dword v18, v6, s[8:9]
	v_add_u32_e32 v6, 0x21200, v11
	global_load_dword v19, v6, s[8:9]
	v_add_u32_e32 v6, 0xd000, v11
	global_load_dword v20, v6, s[8:9]
	v_add_u32_e32 v6, 0x21400, v11
	global_load_dword v21, v6, s[8:9]
	v_add_u32_e32 v6, 0xd200, v11
	global_load_dword v22, v6, s[8:9]
	v_add_u32_e32 v6, 0x21600, v11
	global_load_dword v23, v6, s[8:9]
	v_add_u32_e32 v6, 0xd400, v11
	global_load_dword v24, v6, s[8:9]
	v_add_u32_e32 v6, 0x21800, v11
	global_load_dword v25, v6, s[8:9]
	v_add_u32_e32 v6, 0xd600, v11
	global_load_dword v26, v6, s[8:9]
	v_add_u32_e32 v6, 0x21a00, v11
	global_load_dword v27, v6, s[8:9]
	v_add_u32_e32 v6, 0xde00, v12
	global_load_dword v28, v6, s[8:9]
	v_add_u32_e32 v6, 0xe000, v12
	global_load_dword v29, v6, s[8:9]
	v_add_u32_e32 v6, 0xe200, v12
	global_load_dword v30, v6, s[8:9]
	v_add_u32_e32 v6, 0x1a00, v4
	global_load_dword v31, v6, s[8:9]
	s_waitcnt vmcnt(15)
	v_mul_f32_e32 v16, 0x41800000, v16
	s_waitcnt vmcnt(14)
	v_mul_f32_e32 v17, 0x41000000, v17
	s_waitcnt vmcnt(13)
	v_mul_f32_e32 v18, 0x41800000, v18
	s_waitcnt vmcnt(12)
	v_mul_f32_e32 v19, 0x41000000, v19
	s_waitcnt vmcnt(11)
	v_mul_f32_e32 v20, 0x41800000, v20
	s_waitcnt vmcnt(10)
	v_mul_f32_e32 v21, 0x41000000, v21
	s_waitcnt vmcnt(9)
	v_mul_f32_e32 v22, 0x41800000, v22
	s_waitcnt vmcnt(8)
	v_mul_f32_e32 v23, 0x41000000, v23
	s_waitcnt vmcnt(7)
	v_mul_f32_e32 v24, 0x41800000, v24
	s_waitcnt vmcnt(6)
	v_mul_f32_e32 v25, 0x41000000, v25
	s_waitcnt vmcnt(5)
	v_mul_f32_e32 v26, 0x41800000, v26
	s_waitcnt vmcnt(4)
	v_mul_f32_e32 v27, 0x41000000, v27
	s_waitcnt vmcnt(3)
	v_mul_f32_e32 v28, v9, v28
	s_waitcnt vmcnt(2)
	v_mul_f32_e32 v29, v9, v29
	s_waitcnt vmcnt(1)
	v_mul_f32_e32 v30, v9, v30
	s_waitcnt vmcnt(0)
	v_mul_f32_e32 v31, v10, v31
	v_cvt_pk_fp8_f32 v0, v16, v17
	v_cvt_pk_fp8_f32 v1, v20, v21
	v_cvt_pk_fp8_f32 v2, v24, v25
	v_cvt_pk_fp8_f32 v3, v28, v29
	v_cvt_pk_fp8_f32 v0, v18, v19 op_sel:[0,0,1]
	v_cvt_pk_fp8_f32 v1, v22, v23 op_sel:[0,0,1]
	v_cvt_pk_fp8_f32 v2, v26, v27 op_sel:[0,0,1]
	v_cvt_pk_fp8_f32 v3, v30, v31 op_sel:[0,0,1]
	s_nop 1
	global_store_dwordx4 v5, v[0:3], s[6:7]
	s_endpgm
.Lw1_C:
	v_mov_b32_e32 v0, 0
	v_mov_b32_e32 v1, 0
	v_mov_b32_e32 v2, 0
	v_mov_b32_e32 v3, 0
	global_store_dwordx4 v5, v[0:3], s[6:7]
	s_endpgm
